# v12_xrmerge
# baseline (speedup 1.0000x reference)
.LBB1_127:
	ds_read2_b32 v[70:71], v68 offset1:4
	ds_read2_b32 v[166:167], v68 offset0:8 offset1:12
	ds_read_b32 v69, v67
	ds_read_b32 v72, v67 offset:1088
	ds_read_b32 v73, v67 offset:2176
	ds_read_b32 v107, v67 offset:3264
	s_add_i32 s55, s55, 1
	v_add_u32_e32 v67, 0x1100, v67
	s_cmp_lt_u32 s55, 2
	v_add_u32_e32 v68, 64, v68
	s_waitcnt lgkmcnt(0)
	v_mfma_f32_16x16x4_f32 a[0:3], v70, v69, a[0:3]
	v_mfma_f32_16x16x4_f32 a[0:3], v71, v72, a[0:3]
	v_mfma_f32_16x16x4_f32 a[0:3], v166, v73, a[0:3]
	v_mfma_f32_16x16x4_f32 a[0:3], v167, v107, a[0:3]
	s_cbranch_scc1 .LBB1_127
	v_add_u32_e32 v66, v66, v129
	ds_read_b128 v[66:69], v66 offset:192
	s_waitcnt lgkmcnt(0)
	s_nop 5
	v_mfma_f32_16x16x4_f32 a[4:7], v66, a0, 0
	v_mul_u32_u24_e32 v66, 0x440, v127
	v_add3_u32 v66, s54, v128, v66
	v_mfma_f32_16x16x4_f32 a[4:7], v67, a1, a[4:7]
	v_add_u32_e32 v67, 0x3200, v66
	v_add_u32_e32 v66, 0x3400, v66
	v_mfma_f32_16x16x4_f32 a[4:7], v68, a2, a[4:7]
	v_mfma_f32_16x16x4_f32 a[0:3], v69, a3, a[4:7]
	s_nop 9
	v_accvgpr_read_b32 v68, a0
	v_accvgpr_read_b32 v69, a1
	v_accvgpr_read_b32 v70, a2
	v_accvgpr_read_b32 v71, a3
	v_xor_b32_e32 v68, 0x80000000, v68
	v_xor_b32_e32 v69, 0x80000000, v69
	v_xor_b32_e32 v70, 0x80000000, v70
	v_xor_b32_e32 v71, 0x80000000, v71
	ds_write2_b32 v67, v68, v69 offset0:64 offset1:132
	ds_write2_b32 v66, v70, v71 offset0:72 offset1:140

.LBB1_248:
	ds_read2_b32 v[6:7], v4 offset1:4
	ds_read2_b32 v[16:17], v4 offset0:8 offset1:12
	ds_read_b32 v5, v3
	ds_read_b32 v8, v3 offset:1088
	ds_read_b32 v9, v3 offset:2176
	ds_read_b32 v10, v3 offset:3264
	s_add_i32 s69, s69, 1
	v_add_u32_e32 v3, 0x1100, v3
	s_cmp_lt_u32 s69, 2
	v_add_u32_e32 v4, 64, v4
	s_waitcnt lgkmcnt(0)
	v_mfma_f32_16x16x4_f32 a[0:3], v6, v5, a[0:3]
	v_mfma_f32_16x16x4_f32 a[0:3], v7, v8, a[0:3]
	v_mfma_f32_16x16x4_f32 a[0:3], v16, v9, a[0:3]
	v_mfma_f32_16x16x4_f32 a[0:3], v17, v10, a[0:3]
	s_cbranch_scc1 .LBB1_248
	v_add_u32_e32 v2, v2, v129
	ds_read_b128 v[2:5], v2 offset:192
	s_waitcnt lgkmcnt(0)
	s_nop 5
	v_mfma_f32_16x16x4_f32 a[4:7], v2, a0, 0
	v_mul_u32_u24_e32 v2, 0x440, v127
	v_add3_u32 v2, s2, v128, v2
	v_mfma_f32_16x16x4_f32 a[4:7], v3, a1, a[4:7]
	v_add_u32_e32 v3, 0x3200, v2
	v_add_u32_e32 v2, 0x3400, v2
	v_mfma_f32_16x16x4_f32 a[4:7], v4, a2, a[4:7]
	v_mfma_f32_16x16x4_f32 a[0:3], v5, a3, a[4:7]
	s_nop 9
	v_accvgpr_read_b32 v4, a0
	v_accvgpr_read_b32 v5, a1
	v_accvgpr_read_b32 v6, a2
	v_accvgpr_read_b32 v7, a3
	v_xor_b32_e32 v4, 0x80000000, v4
	v_xor_b32_e32 v5, 0x80000000, v5
	v_xor_b32_e32 v6, 0x80000000, v6
	v_xor_b32_e32 v7, 0x80000000, v7
	ds_write2_b32 v3, v4, v5 offset0:64 offset1:132
	ds_write2_b32 v2, v6, v7 offset0:72 offset1:140

.LBB1_318:
	ds_read2_b32 v[4:5], v3 offset1:4
	ds_read2_b32 v[54:55], v3 offset0:8 offset1:12
	ds_read_b32 v6, v2
	ds_read_b32 v7, v2 offset:1088
	ds_read_b32 v8, v2 offset:2176
	ds_read_b32 v9, v2 offset:3264
	s_add_i32 s53, s53, 1
	v_add_u32_e32 v2, 0x1100, v2
	s_cmp_lt_u32 s53, 2
	v_add_u32_e32 v3, 64, v3
	s_waitcnt lgkmcnt(0)
	v_mfma_f32_16x16x4_f32 a[0:3], v4, v6, a[0:3]
	v_mfma_f32_16x16x4_f32 a[0:3], v5, v7, a[0:3]
	v_mfma_f32_16x16x4_f32 a[0:3], v54, v8, a[0:3]
	v_mfma_f32_16x16x4_f32 a[0:3], v55, v9, a[0:3]
	s_cbranch_scc1 .LBB1_318
	v_add_u32_e32 v1, v1, v17
	ds_read_b128 v[2:5], v1 offset:192
	v_mul_u32_u24_e32 v1, 0x440, v15
	v_add3_u32 v1, s52, v16, v1
	s_waitcnt lgkmcnt(0)
	s_nop 3
	v_mfma_f32_16x16x4_f32 a[4:7], v2, a0, 0
	v_add_u32_e32 v2, 0x3200, v1
	v_add_u32_e32 v1, 0x3400, v1
	v_mfma_f32_16x16x4_f32 a[4:7], v3, a1, a[4:7]
	v_mfma_f32_16x16x4_f32 a[4:7], v4, a2, a[4:7]
	v_mfma_f32_16x16x4_f32 a[0:3], v5, a3, a[4:7]
	s_nop 9
	v_accvgpr_read_b32 v3, a0
	v_accvgpr_read_b32 v4, a1
	v_accvgpr_read_b32 v5, a2
	v_accvgpr_read_b32 v6, a3
	v_xor_b32_e32 v3, 0x80000000, v3
	v_xor_b32_e32 v4, 0x80000000, v4
	v_xor_b32_e32 v5, 0x80000000, v5
	v_xor_b32_e32 v6, 0x80000000, v6
	ds_write2_b32 v2, v3, v4 offset0:64 offset1:132
	ds_write2_b32 v1, v5, v6 offset0:72 offset1:140

.LBB1_359:
	ds_read2_b32 v[4:5], v2 offset1:4
	ds_read2_b32 v[36:37], v2 offset0:8 offset1:12
	ds_read_b32 v3, v1
	ds_read_b32 v6, v1 offset:1088
	ds_read_b32 v7, v1 offset:2176
	ds_read_b32 v8, v1 offset:3264
	s_add_i32 s70, s70, 1
	v_add_u32_e32 v1, 0x1100, v1
	s_cmp_lt_u32 s70, 2
	v_add_u32_e32 v2, 64, v2
	s_waitcnt lgkmcnt(0)
	v_mfma_f32_16x16x4_f32 a[0:3], v4, v3, a[0:3]
	v_mfma_f32_16x16x4_f32 a[0:3], v5, v6, a[0:3]
	v_mfma_f32_16x16x4_f32 a[0:3], v36, v7, a[0:3]
	v_mfma_f32_16x16x4_f32 a[0:3], v37, v8, a[0:3]
	s_cbranch_scc1 .LBB1_359
	v_add_u32_e32 v0, v0, v17
	ds_read_b128 v[0:3], v0 offset:192
	s_waitcnt lgkmcnt(0)
	s_nop 5
	v_mfma_f32_16x16x4_f32 a[4:7], v0, a0, 0
	v_mul_u32_u24_e32 v0, 0x440, v15
	v_add3_u32 v0, s0, v16, v0
	v_mfma_f32_16x16x4_f32 a[4:7], v1, a1, a[4:7]
	v_add_u32_e32 v1, 0x3200, v0
	v_add_u32_e32 v0, 0x3400, v0
	v_mfma_f32_16x16x4_f32 a[4:7], v2, a2, a[4:7]
	v_mfma_f32_16x16x4_f32 a[0:3], v3, a3, a[4:7]
	s_nop 9
	v_accvgpr_read_b32 v2, a0
	v_accvgpr_read_b32 v3, a1
	v_accvgpr_read_b32 v4, a2
	v_accvgpr_read_b32 v5, a3
	v_xor_b32_e32 v2, 0x80000000, v2
	v_xor_b32_e32 v3, 0x80000000, v3
	v_xor_b32_e32 v4, 0x80000000, v4
	v_xor_b32_e32 v5, 0x80000000, v5
	ds_write2_b32 v1, v2, v3 offset0:64 offset1:132
	ds_write2_b32 v0, v4, v5 offset0:72 offset1:140
